# attention Q fragment loads marked nt (read once)
# baseline (speedup 1.0000x reference)
_ZN3att8attn_fwdEPKDF16_PDF16_:
	s_load_dwordx4 s[4:7], s[0:1], 0x0
	s_lshl_b32 s0, s2, 2
	s_and_b32 s0, s0, 28
	s_lshr_b32 s1, s2, 6
	v_readfirstlane_b32 s10, v0
	s_add_i32 s8, s0, s1
	s_lshl_b32 s0, s2, 5
	s_mov_b32 s9, 0
	s_lshr_b32 s26, s10, 6
	s_and_b32 s27, s0, 0x700
	s_lshl_b64 s[0:1], s[8:9], 11
	s_or_b32 s0, s0, s27
	s_lshl_b32 s28, s26, 5
	s_add_u32 s0, s0, s28
	s_addc_u32 s1, s1, 0
	s_lshl_b64 s[0:1], s[0:1], 7
	s_waitcnt lgkmcnt(0)
	s_add_u32 s12, s4, s0
	s_addc_u32 s13, s5, s1
	s_lshl_b64 s[2:3], s[8:9], 18
	s_add_u32 s1, s4, s2
	s_addc_u32 s15, s5, s3
	s_and_b32 s0, s10, 0x3fffffc0
	s_lshl_b32 s10, s26, 9
	s_mov_b32 s11, s9
	s_lshl_b64 s[10:11], s[10:11], 1
	v_and_b32_e32 v190, 63, v0
	s_add_u32 s14, s1, s10
	s_addc_u32 s15, s15, s11
	v_lshlrev_b32_e32 v184, 4, v190
	v_mov_b32_e32 v185, 0
	v_lshl_add_u64 v[48:49], s[14:15], 0, v[184:185]
	s_mov_b64 s[14:15], 0x800000
	s_lshl_b32 s1, s26, 10
	v_lshl_add_u64 v[180:181], v[48:49], 0, s[14:15]
	s_mov_b64 s[14:15], 0x1000000
	s_cmp_lg_u32 0, -1
	v_lshl_add_u64 v[182:183], v[48:49], 0, s[14:15]
	s_cselect_b32 s14, 0, 0
	v_bfe_u32 v192, v0, 5, 1
	s_add_i32 s30, s1, s14
	s_mov_b32 s1, m0
	s_mov_b32 m0, s30
	s_nop 0
	global_load_lds_dwordx4 v[180:181], off
	s_mov_b32 m0, s1
	v_and_b32_e32 v191, 31, v0
	s_add_i32 s31, s30, 0x6000
	s_mov_b32 s1, m0
	s_mov_b32 m0, s31
	s_nop 0
	global_load_lds_dwordx4 v[182:183], off
	s_mov_b32 m0, s1
	s_mov_b64 s[14:15], 0x802000
	v_lshlrev_b32_e32 v195, 4, v192
	v_lshl_add_u64 v[2:3], v[48:49], 0, s[14:15]
	s_add_i32 s1, s30, 0x2000
	s_mov_b32 s14, m0
	s_mov_b32 m0, s1
	s_nop 0
	global_load_lds_dwordx4 v[2:3], off
	s_mov_b32 m0, s14
	v_lshl_or_b32 v1, v191, 7, v195
	global_load_dwordx4 v[136:139], v1, s[12:13] nt
	global_load_dwordx4 v[128:131], v1, s[12:13] offset:32 nt
	global_load_dwordx4 v[120:123], v1, s[12:13] offset:64 nt
	global_load_dwordx4 v[116:119], v1, s[12:13] offset:96 nt
	s_mov_b64 s[14:15], 0x804000
	v_mov_b32_e32 v2, v185
	v_mov_b32_e32 v3, v185
	v_mov_b32_e32 v4, v185
	v_mov_b32_e32 v5, v185
	v_mov_b32_e32 v6, v185
	v_mov_b32_e32 v7, v185
	v_mov_b32_e32 v8, v185
	v_mov_b32_e32 v9, v185
	v_mov_b32_e32 v10, v185
	v_mov_b32_e32 v11, v185
	v_mov_b32_e32 v12, v185
	v_mov_b32_e32 v13, v185
	v_mov_b32_e32 v14, v185
	v_mov_b32_e32 v15, v185
	v_mov_b32_e32 v16, v185
	v_mov_b32_e32 v17, v185
	v_lshlrev_b32_e32 v1, 10, v192
	v_lshlrev_b32_e32 v18, 4, v191
	v_add3_u32 v198, 0, v1, v18
	v_lshl_add_u64 v[18:19], v[48:49], 0, s[14:15]
	s_add_i32 s1, s30, 0x4000
	s_mov_b32 s12, m0
	s_mov_b32 m0, s1
	s_nop 0
	global_load_lds_dwordx4 v[18:19], off
	s_mov_b32 m0, s12
	s_waitcnt vmcnt(3) lgkmcnt(0)
	s_barrier
	ds_read_b128 v[34:37], v198
	ds_read_b128 v[38:41], v198 offset:512
	v_lshlrev_b32_e32 v193, 3, v0
	s_mov_b64 s[16:17], 0x1002000
	s_add_i32 s1, s30, 0x8000
	s_lshl_b32 s0, s0, 2
	s_add_i32 s29, s0, 0
	s_add_u32 s2, s10, s2
	s_addc_u32 s3, s11, s3
	s_mov_b32 s20, -1
	s_movk_i32 s23, 0x2000
	s_movk_i32 s21, 0x4000
	s_mov_b64 s[10:11], 0x2000
	s_mov_b32 s22, 0x41000000
	s_mov_b64 s[14:15], 0x4000
	v_lshl_add_u32 v196, v191, 2, s29
	v_mov_b32_e32 v199, 0
	s_waitcnt vmcnt(3) lgkmcnt(1)
	v_mfma_f32_32x32x16_f16 v[18:33], v[34:37], v[136:139], v[2:17]
	s_waitcnt lgkmcnt(0)
	v_mfma_f32_32x32x16_f16 v[2:17], v[38:41], v[136:139], v[2:17]
	ds_read_b128 v[34:37], v198 offset:2048
	ds_read_b128 v[38:41], v198 offset:2560
	s_waitcnt vmcnt(2) lgkmcnt(1)
	v_mfma_f32_32x32x16_f16 v[18:33], v[34:37], v[128:131], v[18:33]
	s_waitcnt lgkmcnt(0)
	v_mfma_f32_32x32x16_f16 v[2:17], v[38:41], v[128:131], v[2:17]
	ds_read_b128 v[34:37], v198 offset:4096
	ds_read_b128 v[38:41], v198 offset:4608
	s_waitcnt vmcnt(1) lgkmcnt(1)
	v_mfma_f32_32x32x16_f16 v[18:33], v[34:37], v[120:123], v[18:33]
	s_waitcnt lgkmcnt(0)
	v_mfma_f32_32x32x16_f16 v[2:17], v[38:41], v[120:123], v[2:17]
	ds_read_b128 v[34:37], v198 offset:6144
	ds_read_b128 v[38:41], v198 offset:6656
	s_waitcnt vmcnt(0) lgkmcnt(1)
	v_mfma_f32_32x32x16_f16 v[18:33], v[34:37], v[116:119], v[18:33]
	s_waitcnt lgkmcnt(0)
	v_mfma_f32_32x32x16_f16 v[2:17], v[38:41], v[116:119], v[2:17]
	s_nop 9
	v_max_f32_e32 v1, v19, v19
	v_max_f32_e32 v34, v18, v18
	v_max_f32_e32 v1, v34, v1
	v_max3_f32 v35, v20, v21, v3
	v_max3_f32 v1, v1, v2, v4
	v_max3_f32 v34, v35, v24, v25
	v_max3_f32 v1, v1, v5, v22
	v_max3_f32 v34, v34, v8, v9
	v_max3_f32 v1, v1, v23, v6
	v_max3_f32 v34, v34, v28, v29
	v_max3_f32 v1, v1, v7, v26
	v_max3_f32 v34, v34, v12, v13
	v_max3_f32 v1, v1, v27, v10
	v_max3_f32 v34, v34, v32, v33
	v_max3_f32 v1, v1, v11, v30
	v_max3_f32 v34, v34, v16, v17
	v_max3_f32 v1, v1, v31, v14
	v_max3_f32 v1, v1, v15, v34
	v_mov_b32_e32 v34, v1
	s_nop 1
	v_permlane32_swap_b32_e32 v1, v34
	v_max_f32_e32 v34, v34, v34
	v_max_f32_e32 v1, v1, v1
	v_max_f32_e32 v197, v1, v34
	v_lshlrev_b32_e32 v1, 1, v0
	v_sub_f32_e32 v62, v32, v197
	v_and_b32_e32 v1, 32, v1
	v_and_b32_e32 v32, 24, v193
	v_lshlrev_b32_e32 v0, 4, v0
	v_add3_u32 v1, 0, v1, v32
	v_and_b32_e32 v0, 0xc0, v0
	v_lshlrev_b32_e32 v32, 8, v192
	v_add3_u32 v194, v1, v32, v0
	v_xor_b32_e32 v32, 0x80000000, v197
	v_sub_f32_e32 v63, v33, v197
	v_mov_b32_e32 v33, v32
	v_mov_b32_e32 v34, v32
	v_mov_b32_e32 v35, v32
	v_mov_b32_e32 v36, v32
	v_mov_b32_e32 v37, v32
	v_mov_b32_e32 v38, v32
	v_mov_b32_e32 v39, v32
	v_mov_b32_e32 v40, v32
	v_mov_b32_e32 v41, v32
	v_mov_b32_e32 v42, v32
	v_mov_b32_e32 v43, v32
	v_mov_b32_e32 v44, v32
	v_mov_b32_e32 v45, v32
	v_mov_b32_e32 v46, v32
	v_mov_b32_e32 v47, v32
	s_waitcnt vmcnt(0) lgkmcnt(0)
	s_barrier
	v_lshl_add_u64 v[0:1], v[48:49], 0, s[16:17]
	s_mov_b32 s12, m0
	s_mov_b32 m0, s1
	s_nop 0
	global_load_lds_dwordx4 v[0:1], off
	s_mov_b32 m0, s12
	s_mov_b64 s[12:13], 0x806000
	v_lshl_add_u64 v[0:1], v[48:49], 0, s[12:13]
	s_mov_b32 s1, m0
	s_mov_b32 m0, s30
	s_nop 0
	global_load_lds_dwordx4 v[0:1], off
	s_mov_b32 m0, s1
	ds_read_b128 v[172:175], v198 offset:8192
	ds_read_b128 v[168:171], v198 offset:8704
	ds_read_b128 v[164:167], v198 offset:10240
	ds_read_b128 v[160:163], v198 offset:10752
	ds_read_b128 v[156:159], v198 offset:12288
	ds_read_b128 v[152:155], v198 offset:12800
	ds_read_b128 v[148:151], v198 offset:14336
	ds_read_b128 v[144:147], v198 offset:14848
	v_sub_f32_e32 v18, v18, v197
	v_sub_f32_e32 v19, v19, v197
	v_sub_f32_e32 v20, v20, v197
	v_sub_f32_e32 v21, v21, v197
	v_sub_f32_e32 v22, v22, v197
	v_sub_f32_e32 v23, v23, v197
	v_sub_f32_e32 v24, v24, v197
	v_sub_f32_e32 v25, v25, v197
	v_sub_f32_e32 v26, v26, v197
	v_sub_f32_e32 v27, v27, v197
	v_sub_f32_e32 v28, v28, v197
	v_sub_f32_e32 v29, v29, v197
	v_sub_f32_e32 v30, v30, v197
	v_sub_f32_e32 v31, v31, v197
	v_sub_f32_e32 v2, v2, v197
	v_sub_f32_e32 v3, v3, v197
	v_sub_f32_e32 v4, v4, v197
	v_sub_f32_e32 v5, v5, v197
	v_sub_f32_e32 v6, v6, v197
	v_sub_f32_e32 v7, v7, v197
	v_sub_f32_e32 v8, v8, v197
	v_sub_f32_e32 v9, v9, v197
	v_sub_f32_e32 v10, v10, v197
	v_sub_f32_e32 v11, v11, v197
	v_sub_f32_e32 v12, v12, v197
	v_sub_f32_e32 v13, v13, v197
	v_sub_f32_e32 v14, v14, v197
	v_sub_f32_e32 v15, v15, v197
	v_sub_f32_e32 v16, v16, v197
	v_sub_f32_e32 v17, v17, v197
	v_exp_f32_e32 v64, v18
	v_exp_f32_e32 v65, v19
	v_exp_f32_e32 v48, v2
	v_exp_f32_e32 v49, v3
	v_exp_f32_e32 v66, v20
	v_exp_f32_e32 v50, v4
	v_mov_b32_e32 v67, v21
	v_mov_b32_e32 v51, v5
	v_exp_f32_e32 v68, v22
	v_exp_f32_e32 v52, v6
	v_exp_f32_e32 v69, v23
	v_exp_f32_e32 v53, v7
	v_exp_f32_e32 v70, v24
	v_exp_f32_e32 v54, v8
	v_mov_b32_e32 v71, v25
	v_mov_b32_e32 v55, v9
	v_exp_f32_e32 v72, v26
	v_exp_f32_e32 v56, v10
	v_exp_f32_e32 v73, v27
	v_exp_f32_e32 v57, v11
	v_exp_f32_e32 v74, v28
	v_exp_f32_e32 v58, v12
	v_mov_b32_e32 v75, v29
	v_mov_b32_e32 v59, v13
	v_exp_f32_e32 v76, v30
	v_exp_f32_e32 v60, v14
	v_exp_f32_e32 v77, v31
	v_exp_f32_e32 v61, v15
	v_exp_f32_e32 v78, v62
	v_exp_f32_e32 v62, v16
	v_mov_b32_e32 v79, v63
	v_mov_b32_e32 v63, v17
	s_waitcnt vmcnt(2) lgkmcnt(0)
	s_barrier
	v_or_b32_e32 v0, s2, v184
	v_mov_b32_e32 v1, s3
	v_lshl_add_u64 v[186:187], s[4:5], 0, v[0:1]
	s_mov_b32 s2, 0xff800000
	s_mov_b32 s4, 0xff806000
	v_cmp_gt_u32_e64 s[0:1], 32, v190
	s_mov_b32 s3, -1
	s_mov_b32 s5, -1
	s_mov_b64 s[12:13], 0x8000
	v_mov_b32_e32 v0, 0
	v_mov_b32_e32 v1, v185
	v_mov_b32_e32 v2, v185
	v_mov_b32_e32 v3, v185
	v_mov_b32_e32 v4, v185
	v_mov_b32_e32 v5, v185
	v_mov_b32_e32 v6, v185
	v_mov_b32_e32 v7, v185
	v_mov_b32_e32 v8, v185
	v_mov_b32_e32 v9, v185
	v_mov_b32_e32 v10, v185
	v_mov_b32_e32 v11, v185
	v_mov_b32_e32 v12, v185
	v_mov_b32_e32 v13, v185
	v_mov_b32_e32 v14, v185
	v_mov_b32_e32 v15, v185
	v_mov_b32_e32 v16, 0
	v_mov_b32_e32 v17, v185
	v_mov_b32_e32 v18, v185
	v_mov_b32_e32 v19, v185
	v_mov_b32_e32 v20, v185
	v_mov_b32_e32 v21, v185
	v_mov_b32_e32 v22, v185
	v_mov_b32_e32 v23, v185
	v_mov_b32_e32 v24, v185
	v_mov_b32_e32 v25, v185
	v_mov_b32_e32 v26, v185
	v_mov_b32_e32 v27, v185
	v_mov_b32_e32 v28, v185
	v_mov_b32_e32 v29, v185
	v_mov_b32_e32 v30, v185
	v_mov_b32_e32 v31, v185
	v_lshl_add_u64 v[188:189], v[186:187], 0, s[16:17]
